# rope epilogue: bf16 packs written directly into the store quads (62 v_mov removed)
# baseline (speedup 1.0000x reference)
; #define PG8_ST8(rs, b0, p, v) __builtin_amdgcn_raw_buffer_store_b64(v, rs, (int)((const char*)(p) - (const char*)(b0)), 0, 16)
; __device__ __forceinline__ unsigned cvt_pk_bf16(float lo, float hi) { unsigned r; asm volatile("v_cvt_pk_bf16_f32 %0, %1, %2" : "=v"(r) : "v"(lo), "v"(hi)); return r; }
;     __device__ __forceinline__ void operator()(const f32x4 (&acc)[2][2][4][2], const Unit& u, int wr, int wc, int fr, int fq) const {
;     ...
;             const float sc = (pn <= 6 || (pn >= 9 && pn <= 11)) ? qscale : 1.0f;
;             const int f = 16 * (wc & 1) + 4 * fq, col0 = pn * BM + 64 * (wc >> 1) + f;
; #pragma unroll
;             for (int ai = 0; ai < 2; ++ai) {
;                 f32x4 c4[4], s4[4];
; #pragma unroll
;                 for (int m = 0; m < 4; ++m) { const int row = row0 + ai * HALF + m * 16; c4[m] = *(const f32x4*)(rc + (size_t)row * 32 + f); s4[m] = *(const f32x4*)(rs + (size_t)row * 32 + f); }
;                 asm volatile("" ::: "memory");
; #pragma unroll
;                 for (int m = 0; m < 4; ++m) { const int row = row0 + ai * HALF + m * 16;
;                     const f32x4 cc = c4[m] * sc, ss = s4[m] * sc;
;                     bf16_t* rowp = P + (size_t)row * ldp + col0;
; #pragma unroll
;                     for (int bj = 0; bj < 2; ++bj) { const f32x4 x1 = acc[ai][bj][m][0], x2 = acc[ai][bj][m][1]; const f32x4 o1 = x1 * cc - x2 * ss, o2 = x2 * cc + x1 * ss;
;                         u32x2 w1, w2; w1.x = cvt_pk_bf16(o1[0], o1[1]); w1.y = cvt_pk_bf16(o1[2], o1[3]); w2.x = cvt_pk_bf16(o2[0], o2[1]); w2.y = cvt_pk_bf16(o2[2], o2[3]);
;                         PG8_ST8(rsp_, P, rowp + bj * HALF, w1); PG8_ST8(rsp_, P, rowp + bj * HALF + 32, w2); } }
.LBB0_230:
	v_lshl_add_u32 v164, s27, 8, v175
	s_add_i32 s27, s62, s56
	s_cmp_gt_i32 s27, 3
	s_mov_b64 s[34:35], -1
	s_cbranch_scc0 .LBB0_237
	s_cmp_lg_u32 s27, 8
	s_cselect_b64 s[34:35], -1, 0
	s_cmp_lt_u32 s27, 15
	s_cselect_b64 s[36:37], -1, 0
	s_and_b64 s[36:37], s[34:35], s[36:37]
	s_mov_b64 s[34:35], -1
	s_and_b64 vcc, exec, s[36:37]
	v_add_u32_e32 v172, 0x80, v164
	v_add_u32_e32 v170, 0x90, v164
	v_add_u32_e32 v168, 0xa0, v164
	v_add_u32_e32 v166, 0xb0, v164
	s_cbranch_vccz .LBB0_233
	v_lshrrev_b32_e32 v252, 2, v215
	v_and_b32_e32 v245, 15, v215
	v_sub_u32_e32 v252, v252, v245
	v_lshlrev_b32_e32 v245, 4, v245
	v_lshrrev_b32_e32 v246, 4, v215
	v_lshl_or_b32 v245, v246, 2, v245
	v_and_b32_e32 v248, 3, v215
	v_sub_u32_e32 v246, v248, v246
	v_lshlrev_b32_e32 v252, 7, v252
	v_lshl_add_u32 v248, v246, 4, v252
	v_ashrrev_i32_e32 v249, 31, v248
	v_lshl_add_u64 v[246:247], v[154:155], 0, v[248:249]
	v_lshl_add_u64 v[248:249], v[156:157], 0, v[248:249]
	s_cmp_lt_u32 s27, 7
	s_cselect_b64 s[34:35], -1, 0
	s_add_i32 s36, s27, -9
	s_cmp_lt_u32 s36, 3
	s_cselect_b64 s[36:37], -1, 0
	s_or_b64 vcc, s[34:35], s[36:37]
	v_mov_b32_e32 v132, 0x3e38aa3b
	v_ashrrev_i32_e32 v165, 31, v164
	v_cndmask_b32_e32 v174, 1.0, v132, vcc
	v_lshlrev_b64 v[132:133], 7, v[164:165]
	v_lshl_add_u64 v[134:135], v[246:247], 0, v[132:133]
	v_lshl_add_u64 v[132:133], v[248:249], 0, v[132:133]
	global_load_dwordx4 v[176:179], v[134:135], off
	global_load_dwordx4 v[184:187], v[132:133], off
	v_or_b32_e32 v192, 16, v164
	v_ashrrev_i32_e32 v193, 31, v192
	v_lshlrev_b64 v[132:133], 7, v[192:193]
	v_lshl_add_u64 v[134:135], v[246:247], 0, v[132:133]
	v_lshl_add_u64 v[132:133], v[248:249], 0, v[132:133]
	global_load_dwordx4 v[188:191], v[134:135], off
	global_load_dwordx4 v[218:221], v[132:133], off
	v_or_b32_e32 v182, 32, v164
	v_ashrrev_i32_e32 v183, 31, v182
	v_lshlrev_b64 v[132:133], 7, v[182:183]
	v_lshl_add_u64 v[134:135], v[246:247], 0, v[132:133]
	v_lshl_add_u64 v[132:133], v[248:249], 0, v[132:133]
	global_load_dwordx4 v[144:147], v[134:135], off
	global_load_dwordx4 v[140:143], v[132:133], off
	v_or_b32_e32 v180, 48, v164
	v_ashrrev_i32_e32 v181, 31, v180
	v_lshlrev_b64 v[132:133], 7, v[180:181]
	v_lshl_add_u64 v[134:135], v[246:247], 0, v[132:133]
	v_lshl_add_u64 v[132:133], v[248:249], 0, v[132:133]
	global_load_dwordx4 v[136:139], v[134:135], off
	s_movk_i32 s36, 0x2400
	global_load_dwordx4 v[132:135], v[132:133], off
	v_ashrrev_i32_e32 v173, 31, v172
	v_ashrrev_i32_e32 v171, 31, v170
	v_ashrrev_i32_e32 v169, 31, v168
	v_ashrrev_i32_e32 v167, 31, v166
	s_waitcnt vmcnt(0)
	ds_bpermute_b32 v176, v245, v176
	ds_bpermute_b32 v177, v245, v177
	ds_bpermute_b32 v178, v245, v178
	ds_bpermute_b32 v179, v245, v179
	ds_bpermute_b32 v184, v245, v184
	ds_bpermute_b32 v185, v245, v185
	ds_bpermute_b32 v186, v245, v186
	ds_bpermute_b32 v187, v245, v187
	ds_bpermute_b32 v188, v245, v188
	ds_bpermute_b32 v189, v245, v189
	ds_bpermute_b32 v190, v245, v190
	ds_bpermute_b32 v191, v245, v191
	ds_bpermute_b32 v218, v245, v218
	ds_bpermute_b32 v219, v245, v219
	ds_bpermute_b32 v220, v245, v220
	ds_bpermute_b32 v221, v245, v221
	ds_bpermute_b32 v144, v245, v144
	ds_bpermute_b32 v145, v245, v145
	ds_bpermute_b32 v146, v245, v146
	ds_bpermute_b32 v147, v245, v147
	ds_bpermute_b32 v140, v245, v140
	ds_bpermute_b32 v141, v245, v141
	ds_bpermute_b32 v142, v245, v142
	ds_bpermute_b32 v143, v245, v143
	ds_bpermute_b32 v136, v245, v136
	ds_bpermute_b32 v137, v245, v137
	ds_bpermute_b32 v138, v245, v138
	ds_bpermute_b32 v139, v245, v139
	ds_bpermute_b32 v132, v245, v132
	ds_bpermute_b32 v133, v245, v133
	ds_bpermute_b32 v134, v245, v134
	ds_bpermute_b32 v135, v245, v135
	s_waitcnt lgkmcnt(0)
	v_pk_mul_f32 v[198:199], v[174:175], v[178:179] op_sel_hi:[0,1]
	v_pk_mul_f32 v[186:187], v[174:175], v[186:187] op_sel_hi:[0,1]
	v_pk_mul_f32 v[184:185], v[174:175], v[184:185] op_sel_hi:[0,1]
	v_pk_mul_f32 v[200:201], v[174:175], v[176:177] op_sel_hi:[0,1]
	v_mov_b64_e32 v[176:177], s[20:21]
	v_lshrrev_b32_e32 v252, 2, v215
	v_and_b32_e32 v228, 15, v215
	v_sub_u32_e32 v252, v252, v228
	v_mad_i64_i32 v[176:177], s[34:35], v252, s36, v[176:177]
	v_pk_mul_f32 v[208:209], v[118:119], v[186:187]
	v_pk_mul_f32 v[222:223], v[116:117], v[184:185]
	v_mad_i64_i32 v[206:207], s[34:35], v164, s36, v[176:177]
	v_lshl_or_b32 v178, s27, 9, v202
	v_mov_b32_e32 v179, v2
	v_and_b32_e32 v244, 3, v215
	v_lshrrev_b32_e32 v228, 4, v215
	v_sub_u32_e32 v228, v244, v228
	v_lshl_add_u32 v178, v228, 3, v178
	v_and_b32_e32 v228, 1, v215
	v_mad_u32_u24 v178, v228, 56, v178
	v_and_b32_e32 v228, 60, v215
	v_lshl_or_b32 v244, v244, 6, v228
	v_pk_fma_f32 v[208:209], v[126:127], v[198:199], v[208:209] neg_lo:[0,0,1] neg_hi:[0,0,1]
	v_pk_fma_f32 v[222:223], v[124:125], v[200:201], v[222:223] neg_lo:[0,0,1] neg_hi:[0,0,1]
	v_pk_mul_f32 v[224:225], v[126:127], v[186:187]
	v_pk_mul_f32 v[226:227], v[124:125], v[184:185]
	v_lshl_add_u64 v[206:207], v[206:207], 0, v[178:179]
	v_pk_fma_f32 v[224:225], v[118:119], v[198:199], v[224:225]
	v_pk_fma_f32 v[226:227], v[116:117], v[200:201], v[226:227]
	v_cvt_pk_bf16_f32 v228, v222, v223
	v_cvt_pk_bf16_f32 v229, v208, v209
	v_mad_i64_i32 v[192:193], s[34:35], v192, s36, v[176:177]
	v_cvt_pk_bf16_f32 v230, v226, v227
	v_cvt_pk_bf16_f32 v231, v224, v225
	s_nop 1
	v_permlane16_swap_b32_e32 v228, v230
	v_permlane16_swap_b32_e32 v229, v231
	ds_bpermute_b32 v228, v244, v228
	ds_bpermute_b32 v229, v244, v229
	ds_bpermute_b32 v230, v244, v230
	ds_bpermute_b32 v231, v244, v231
	v_pk_mul_f32 v[208:209], v[122:123], v[186:187]
	v_pk_mul_f32 v[222:223], v[120:121], v[184:185]
	v_pk_mul_f32 v[186:187], v[130:131], v[186:187]
	v_pk_mul_f32 v[184:185], v[128:129], v[184:185]
	v_pk_fma_f32 v[186:187], v[122:123], v[198:199], v[186:187]
	v_pk_fma_f32 v[184:185], v[120:121], v[200:201], v[184:185]
	v_pk_fma_f32 v[208:209], v[130:131], v[198:199], v[208:209] neg_lo:[0,0,1] neg_hi:[0,0,1]
	v_pk_fma_f32 v[222:223], v[128:129], v[200:201], v[222:223] neg_lo:[0,0,1] neg_hi:[0,0,1]
	v_lshl_add_u64 v[192:193], v[192:193], 0, v[178:179]
	v_cvt_pk_bf16_f32 v232, v222, v223
	v_cvt_pk_bf16_f32 v233, v208, v209
	v_cvt_pk_bf16_f32 v234, v184, v185
	v_cvt_pk_bf16_f32 v235, v186, v187
	v_pk_mul_f32 v[186:187], v[174:175], v[190:191] op_sel_hi:[0,1]
	v_pk_mul_f32 v[190:191], v[174:175], v[218:219] op_sel_hi:[0,1]
	s_nop 1
	v_permlane16_swap_b32_e32 v232, v234
	v_permlane16_swap_b32_e32 v233, v235
	ds_bpermute_b32 v232, v244, v232
	ds_bpermute_b32 v233, v244, v233
	ds_bpermute_b32 v234, v244, v234
	ds_bpermute_b32 v235, v244, v235
	s_waitcnt lgkmcnt(4)
; #define PG8_ST8(rs, b0, p, v) __builtin_amdgcn_raw_buffer_store_b64(v, rs, (int)((const char*)(p) - (const char*)(b0)), 0, 16)
; __device__ __forceinline__ unsigned cvt_pk_bf16(float lo, float hi) { unsigned r; asm volatile("v_cvt_pk_bf16_f32 %0, %1, %2" : "=v"(r) : "v"(lo), "v"(hi)); return r; }
;     __device__ __forceinline__ void operator()(const f32x4 (&acc)[2][2][4][2], const Unit& u, int wr, int wc, int fr, int fq) const {
;     ...
;                 for (int m = 0; m < 4; ++m) { const int row = row0 + ai * HALF + m * 16;
;                     const f32x4 cc = c4[m] * sc, ss = s4[m] * sc;
;                     bf16_t* rowp = P + (size_t)row * ldp + col0;
; #pragma unroll
;                     for (int bj = 0; bj < 2; ++bj) { const f32x4 x1 = acc[ai][bj][m][0], x2 = acc[ai][bj][m][1]; const f32x4 o1 = x1 * cc - x2 * ss, o2 = x2 * cc + x1 * ss;
;                         u32x2 w1, w2; w1.x = cvt_pk_bf16(o1[0], o1[1]); w1.y = cvt_pk_bf16(o1[2], o1[3]); w2.x = cvt_pk_bf16(o2[0], o2[1]); w2.y = cvt_pk_bf16(o2[2], o2[3]);
;                         PG8_ST8(rsp_, P, rowp + bj * HALF, w1); PG8_ST8(rsp_, P, rowp + bj * HALF + 32, w2); } }
	global_store_dwordx4 v[206:207], v[228:231], off
	v_pk_mul_f32 v[184:185], v[174:175], v[188:189] op_sel_hi:[0,1]
	v_pk_mul_f32 v[188:189], v[174:175], v[220:221] op_sel_hi:[0,1]
	v_pk_mul_f32 v[198:199], v[100:101], v[190:191]
	v_pk_mul_f32 v[200:201], v[102:103], v[188:189]
	v_pk_fma_f32 v[198:199], v[108:109], v[184:185], v[198:199] neg_lo:[0,0,1] neg_hi:[0,0,1]
	v_pk_fma_f32 v[200:201], v[110:111], v[186:187], v[200:201] neg_lo:[0,0,1] neg_hi:[0,0,1]
	v_pk_mul_f32 v[204:205], v[108:109], v[190:191]
	v_pk_mul_f32 v[208:209], v[110:111], v[188:189]
	v_cvt_pk_bf16_f32 v236, v198, v199
	v_cvt_pk_bf16_f32 v237, v200, v201
	v_pk_fma_f32 v[204:205], v[100:101], v[184:185], v[204:205]
	v_pk_fma_f32 v[208:209], v[102:103], v[186:187], v[208:209]
	v_cvt_pk_bf16_f32 v238, v204, v205
	v_pk_mul_f32 v[142:143], v[174:175], v[142:143] op_sel_hi:[0,1]
	v_cvt_pk_bf16_f32 v239, v208, v209
	s_nop 1
	v_permlane16_swap_b32_e32 v236, v238
	v_permlane16_swap_b32_e32 v237, v239
	ds_bpermute_b32 v236, v244, v236
	ds_bpermute_b32 v237, v244, v237
	ds_bpermute_b32 v238, v244, v238
	ds_bpermute_b32 v239, v244, v239
	s_waitcnt lgkmcnt(4)
	global_store_dwordx4 v[206:207], v[232:235], off offset:256
	v_pk_mul_f32 v[198:199], v[104:105], v[190:191]
	v_pk_mul_f32 v[190:191], v[112:113], v[190:191]
	v_pk_mul_f32 v[200:201], v[106:107], v[188:189]
	v_pk_fma_f32 v[198:199], v[112:113], v[184:185], v[198:199] neg_lo:[0,0,1] neg_hi:[0,0,1]
	v_pk_mul_f32 v[188:189], v[114:115], v[188:189]
	v_pk_fma_f32 v[184:185], v[104:105], v[184:185], v[190:191]
	v_pk_fma_f32 v[200:201], v[114:115], v[186:187], v[200:201] neg_lo:[0,0,1] neg_hi:[0,0,1]
	v_pk_fma_f32 v[186:187], v[106:107], v[186:187], v[188:189]
	v_cvt_pk_bf16_f32 v240, v198, v199
	v_cvt_pk_bf16_f32 v241, v200, v201
	v_cvt_pk_bf16_f32 v242, v184, v185
	v_pk_mul_f32 v[140:141], v[174:175], v[140:141] op_sel_hi:[0,1]
	v_cvt_pk_bf16_f32 v243, v186, v187
	s_nop 1
	v_permlane16_swap_b32_e32 v240, v242
	v_permlane16_swap_b32_e32 v241, v243
	ds_bpermute_b32 v240, v244, v240
	ds_bpermute_b32 v241, v244, v241
	ds_bpermute_b32 v242, v244, v242
	ds_bpermute_b32 v243, v244, v243
	s_waitcnt lgkmcnt(4)
	global_store_dwordx4 v[192:193], v[236:239], off
	v_pk_mul_f32 v[144:145], v[174:175], v[144:145] op_sel_hi:[0,1]
	v_pk_mul_f32 v[146:147], v[174:175], v[146:147] op_sel_hi:[0,1]
	v_pk_mul_f32 v[184:185], v[84:85], v[140:141]
	v_pk_mul_f32 v[186:187], v[86:87], v[142:143]
	v_mad_i64_i32 v[182:183], s[34:35], v182, s36, v[176:177]
	v_pk_fma_f32 v[186:187], v[94:95], v[146:147], v[186:187] neg_lo:[0,0,1] neg_hi:[0,0,1]
	v_pk_fma_f32 v[184:185], v[92:93], v[144:145], v[184:185] neg_lo:[0,0,1] neg_hi:[0,0,1]
	v_pk_mul_f32 v[188:189], v[92:93], v[140:141]
	v_pk_mul_f32 v[190:191], v[94:95], v[142:143]
	v_lshl_add_u64 v[182:183], v[182:183], 0, v[178:179]
	v_pk_fma_f32 v[190:191], v[86:87], v[146:147], v[190:191]
	v_pk_fma_f32 v[188:189], v[84:85], v[144:145], v[188:189]
	v_cvt_pk_bf16_f32 v228, v184, v185
	v_cvt_pk_bf16_f32 v229, v186, v187
	v_pk_mul_f32 v[134:135], v[174:175], v[134:135] op_sel_hi:[0,1]
	v_cvt_pk_bf16_f32 v230, v188, v189
	v_cvt_pk_bf16_f32 v231, v190, v191
	s_nop 1
	v_permlane16_swap_b32_e32 v228, v230
	v_permlane16_swap_b32_e32 v229, v231
	ds_bpermute_b32 v228, v244, v228
	ds_bpermute_b32 v229, v244, v229
	ds_bpermute_b32 v230, v244, v230
	ds_bpermute_b32 v231, v244, v231
	s_waitcnt lgkmcnt(4)
	global_store_dwordx4 v[192:193], v[240:243], off offset:256
	v_pk_mul_f32 v[184:185], v[88:89], v[140:141]
	v_pk_mul_f32 v[186:187], v[90:91], v[142:143]
	v_pk_mul_f32 v[140:141], v[96:97], v[140:141]
	v_pk_mul_f32 v[142:143], v[98:99], v[142:143]
	v_pk_fma_f32 v[186:187], v[98:99], v[146:147], v[186:187] neg_lo:[0,0,1] neg_hi:[0,0,1]
	v_pk_fma_f32 v[184:185], v[96:97], v[144:145], v[184:185] neg_lo:[0,0,1] neg_hi:[0,0,1]
	v_pk_fma_f32 v[142:143], v[90:91], v[146:147], v[142:143]
	v_pk_fma_f32 v[140:141], v[88:89], v[144:145], v[140:141]
	v_cvt_pk_bf16_f32 v232, v184, v185
	v_cvt_pk_bf16_f32 v233, v186, v187
	v_pk_mul_f32 v[132:133], v[174:175], v[132:133] op_sel_hi:[0,1]
	v_cvt_pk_bf16_f32 v234, v140, v141
	v_cvt_pk_bf16_f32 v235, v142, v143
	s_nop 1
	v_permlane16_swap_b32_e32 v232, v234
	v_permlane16_swap_b32_e32 v233, v235
	ds_bpermute_b32 v232, v244, v232
	ds_bpermute_b32 v233, v244, v233
	ds_bpermute_b32 v234, v244, v234
	ds_bpermute_b32 v235, v244, v235
	s_waitcnt lgkmcnt(4)
	global_store_dwordx4 v[182:183], v[228:231], off
	v_pk_mul_f32 v[136:137], v[174:175], v[136:137] op_sel_hi:[0,1]
	v_pk_mul_f32 v[138:139], v[174:175], v[138:139] op_sel_hi:[0,1]
	v_pk_mul_f32 v[142:143], v[68:69], v[132:133]
	v_pk_mul_f32 v[144:145], v[70:71], v[134:135]
	v_mad_i64_i32 v[140:141], s[34:35], v180, s36, v[176:177]
	v_pk_fma_f32 v[144:145], v[78:79], v[138:139], v[144:145] neg_lo:[0,0,1] neg_hi:[0,0,1]
	v_pk_fma_f32 v[142:143], v[76:77], v[136:137], v[142:143] neg_lo:[0,0,1] neg_hi:[0,0,1]
	v_pk_mul_f32 v[146:147], v[76:77], v[132:133]
	v_pk_mul_f32 v[180:181], v[78:79], v[134:135]
	v_lshl_add_u64 v[140:141], v[140:141], 0, v[178:179]
	v_pk_fma_f32 v[180:181], v[70:71], v[138:139], v[180:181]
	v_pk_fma_f32 v[146:147], v[68:69], v[136:137], v[146:147]
	v_cvt_pk_bf16_f32 v236, v142, v143
	v_cvt_pk_bf16_f32 v237, v144, v145
	v_lshlrev_b64 v[184:185], 7, v[168:169]
	v_cvt_pk_bf16_f32 v238, v146, v147
	v_cvt_pk_bf16_f32 v239, v180, v181
	s_nop 1
	v_permlane16_swap_b32_e32 v236, v238
	v_permlane16_swap_b32_e32 v237, v239
	ds_bpermute_b32 v236, v244, v236
	ds_bpermute_b32 v237, v244, v237
	ds_bpermute_b32 v238, v244, v238
	ds_bpermute_b32 v239, v244, v239
	s_waitcnt lgkmcnt(4)
; #define PG8_ST8(rs, b0, p, v) __builtin_amdgcn_raw_buffer_store_b64(v, rs, (int)((const char*)(p) - (const char*)(b0)), 0, 16)
; __device__ __forceinline__ unsigned cvt_pk_bf16(float lo, float hi) { unsigned r; asm volatile("v_cvt_pk_bf16_f32 %0, %1, %2" : "=v"(r) : "v"(lo), "v"(hi)); return r; }
;     __device__ __forceinline__ void operator()(const f32x4 (&acc)[2][2][4][2], const Unit& u, int wr, int wc, int fr, int fq) const {
;     ...
;             for (int ai = 0; ai < 2; ++ai) {
;                 f32x4 c4[4], s4[4];
; #pragma unroll
;                 for (int m = 0; m < 4; ++m) { const int row = row0 + ai * HALF + m * 16; c4[m] = *(const f32x4*)(rc + (size_t)row * 32 + f); s4[m] = *(const f32x4*)(rs + (size_t)row * 32 + f); }
;                 asm volatile("" ::: "memory");
; #pragma unroll
;                 for (int m = 0; m < 4; ++m) { const int row = row0 + ai * HALF + m * 16;
;                     const f32x4 cc = c4[m] * sc, ss = s4[m] * sc;
;                     bf16_t* rowp = P + (size_t)row * ldp + col0;
; #pragma unroll
;                     for (int bj = 0; bj < 2; ++bj) { const f32x4 x1 = acc[ai][bj][m][0], x2 = acc[ai][bj][m][1]; const f32x4 o1 = x1 * cc - x2 * ss, o2 = x2 * cc + x1 * ss;
;                         u32x2 w1, w2; w1.x = cvt_pk_bf16(o1[0], o1[1]); w1.y = cvt_pk_bf16(o1[2], o1[3]); w2.x = cvt_pk_bf16(o2[0], o2[1]); w2.y = cvt_pk_bf16(o2[2], o2[3]);
;                         PG8_ST8(rsp_, P, rowp + bj * HALF, w1); PG8_ST8(rsp_, P, rowp + bj * HALF + 32, w2); } }
	global_store_dwordx4 v[182:183], v[232:235], off offset:256
	v_pk_mul_f32 v[142:143], v[72:73], v[132:133]
	v_pk_mul_f32 v[144:145], v[74:75], v[134:135]
	v_pk_mul_f32 v[132:133], v[80:81], v[132:133]
	v_pk_fma_f32 v[144:145], v[82:83], v[138:139], v[144:145] neg_lo:[0,0,1] neg_hi:[0,0,1]
	v_pk_fma_f32 v[142:143], v[80:81], v[136:137], v[142:143] neg_lo:[0,0,1] neg_hi:[0,0,1]
	v_pk_mul_f32 v[134:135], v[82:83], v[134:135]
	v_pk_fma_f32 v[132:133], v[72:73], v[136:137], v[132:133]
	v_cvt_pk_bf16_f32 v240, v142, v143
	v_cvt_pk_bf16_f32 v241, v144, v145
	v_pk_fma_f32 v[134:135], v[74:75], v[138:139], v[134:135]
	v_cvt_pk_bf16_f32 v242, v132, v133
	v_lshlrev_b64 v[144:145], 7, v[170:171]
	v_cvt_pk_bf16_f32 v243, v134, v135
	s_nop 1
	v_permlane16_swap_b32_e32 v240, v242
	v_permlane16_swap_b32_e32 v241, v243
	ds_bpermute_b32 v240, v244, v240
	ds_bpermute_b32 v241, v244, v241
	ds_bpermute_b32 v242, v244, v242
	ds_bpermute_b32 v243, v244, v243
	s_waitcnt lgkmcnt(4)
	global_store_dwordx4 v[140:141], v[236:239], off
	s_waitcnt lgkmcnt(0)
	global_store_dwordx4 v[140:141], v[240:243], off offset:256
	v_lshlrev_b64 v[136:137], 7, v[172:173]
	v_lshl_add_u64 v[132:133], v[246:247], 0, v[136:137]
	v_lshl_add_u64 v[136:137], v[248:249], 0, v[136:137]
	global_load_dwordx4 v[132:135], v[132:133], off
	v_lshl_add_u64 v[140:141], v[246:247], 0, v[144:145]
	global_load_dwordx4 v[136:139], v[136:137], off
	v_lshl_add_u64 v[144:145], v[248:249], 0, v[144:145]
	global_load_dwordx4 v[140:143], v[140:141], off
	v_lshl_add_u64 v[180:181], v[246:247], 0, v[184:185]
	global_load_dwordx4 v[144:147], v[144:145], off
	v_lshl_add_u64 v[184:185], v[248:249], 0, v[184:185]
	global_load_dwordx4 v[180:183], v[180:181], off
	v_lshlrev_b64 v[192:193], 7, v[166:167]
	global_load_dwordx4 v[184:187], v[184:185], off
	v_lshl_add_u64 v[188:189], v[246:247], 0, v[192:193]
	v_lshl_add_u64 v[192:193], v[248:249], 0, v[192:193]
	global_load_dwordx4 v[188:191], v[188:189], off
	global_load_dwordx4 v[218:221], v[192:193], off
	s_waitcnt vmcnt(0)
	ds_bpermute_b32 v132, v245, v132
	ds_bpermute_b32 v133, v245, v133
	ds_bpermute_b32 v134, v245, v134
	ds_bpermute_b32 v135, v245, v135
	ds_bpermute_b32 v136, v245, v136
	ds_bpermute_b32 v137, v245, v137
	ds_bpermute_b32 v138, v245, v138
	ds_bpermute_b32 v139, v245, v139
	ds_bpermute_b32 v140, v245, v140
	ds_bpermute_b32 v141, v245, v141
	ds_bpermute_b32 v142, v245, v142
	ds_bpermute_b32 v143, v245, v143
	ds_bpermute_b32 v144, v245, v144
	ds_bpermute_b32 v145, v245, v145
	ds_bpermute_b32 v146, v245, v146
	ds_bpermute_b32 v147, v245, v147
	ds_bpermute_b32 v180, v245, v180
	ds_bpermute_b32 v181, v245, v181
	ds_bpermute_b32 v182, v245, v182
	ds_bpermute_b32 v183, v245, v183
	ds_bpermute_b32 v184, v245, v184
	ds_bpermute_b32 v185, v245, v185
	ds_bpermute_b32 v186, v245, v186
	ds_bpermute_b32 v187, v245, v187
	ds_bpermute_b32 v188, v245, v188
	ds_bpermute_b32 v189, v245, v189
	ds_bpermute_b32 v190, v245, v190
	ds_bpermute_b32 v191, v245, v191
	ds_bpermute_b32 v218, v245, v218
	ds_bpermute_b32 v219, v245, v219
	ds_bpermute_b32 v220, v245, v220
	ds_bpermute_b32 v221, v245, v221
	s_waitcnt lgkmcnt(0)
	v_pk_mul_f32 v[132:133], v[174:175], v[132:133] op_sel_hi:[0,1]
	v_pk_mul_f32 v[138:139], v[174:175], v[138:139] op_sel_hi:[0,1]
	v_pk_mul_f32 v[136:137], v[174:175], v[136:137] op_sel_hi:[0,1]
	v_pk_mul_f32 v[134:135], v[174:175], v[134:135] op_sel_hi:[0,1]
	v_pk_mul_f32 v[198:199], v[52:53], v[136:137]
	v_pk_mul_f32 v[200:201], v[54:55], v[138:139]
	v_mad_i64_i32 v[206:207], s[34:35], v172, s36, v[176:177]
	v_pk_fma_f32 v[200:201], v[62:63], v[134:135], v[200:201] neg_lo:[0,0,1] neg_hi:[0,0,1]
	v_pk_fma_f32 v[198:199], v[60:61], v[132:133], v[198:199] neg_lo:[0,0,1] neg_hi:[0,0,1]
	v_pk_mul_f32 v[204:205], v[60:61], v[136:137]
	v_pk_mul_f32 v[208:209], v[62:63], v[138:139]
	v_lshl_add_u64 v[206:207], v[206:207], 0, v[178:179]
	v_pk_fma_f32 v[208:209], v[54:55], v[134:135], v[208:209]
	v_pk_fma_f32 v[204:205], v[52:53], v[132:133], v[204:205]
	v_cvt_pk_bf16_f32 v228, v198, v199
	v_cvt_pk_bf16_f32 v229, v200, v201
	s_nop 0
	v_cvt_pk_bf16_f32 v230, v204, v205
	v_cvt_pk_bf16_f32 v231, v208, v209
	s_nop 1
	v_permlane16_swap_b32_e32 v228, v230
	v_permlane16_swap_b32_e32 v229, v231
	ds_bpermute_b32 v228, v244, v228
	ds_bpermute_b32 v229, v244, v229
	ds_bpermute_b32 v230, v244, v230
	ds_bpermute_b32 v231, v244, v231
	v_pk_mul_f32 v[198:199], v[56:57], v[136:137]
	v_pk_mul_f32 v[200:201], v[58:59], v[138:139]
	v_pk_mul_f32 v[136:137], v[64:65], v[136:137]
	v_pk_fma_f32 v[200:201], v[66:67], v[134:135], v[200:201] neg_lo:[0,0,1] neg_hi:[0,0,1]
	v_pk_fma_f32 v[198:199], v[64:65], v[132:133], v[198:199] neg_lo:[0,0,1] neg_hi:[0,0,1]
	v_pk_mul_f32 v[138:139], v[66:67], v[138:139]
	v_pk_fma_f32 v[132:133], v[56:57], v[132:133], v[136:137]
	v_cvt_pk_bf16_f32 v232, v198, v199
	v_cvt_pk_bf16_f32 v233, v200, v201
	v_pk_fma_f32 v[134:135], v[58:59], v[134:135], v[138:139]
	v_cvt_pk_bf16_f32 v234, v132, v133
	v_pk_mul_f32 v[138:139], v[174:175], v[144:145] op_sel_hi:[0,1]
	v_cvt_pk_bf16_f32 v235, v134, v135
	s_nop 1
	v_permlane16_swap_b32_e32 v232, v234
	v_permlane16_swap_b32_e32 v233, v235
	ds_bpermute_b32 v232, v244, v232
	ds_bpermute_b32 v233, v244, v233
	ds_bpermute_b32 v234, v244, v234
	ds_bpermute_b32 v235, v244, v235
	s_waitcnt lgkmcnt(4)
; #define PG8_ST8(rs, b0, p, v) __builtin_amdgcn_raw_buffer_store_b64(v, rs, (int)((const char*)(p) - (const char*)(b0)), 0, 16)
; __device__ __forceinline__ unsigned cvt_pk_bf16(float lo, float hi) { unsigned r; asm volatile("v_cvt_pk_bf16_f32 %0, %1, %2" : "=v"(r) : "v"(lo), "v"(hi)); return r; }
;     __device__ __forceinline__ void operator()(const f32x4 (&acc)[2][2][4][2], const Unit& u, int wr, int wc, int fr, int fq) const {
;     ...
;                 for (int m = 0; m < 4; ++m) { const int row = row0 + ai * HALF + m * 16;
;                     const f32x4 cc = c4[m] * sc, ss = s4[m] * sc;
;                     bf16_t* rowp = P + (size_t)row * ldp + col0;
; #pragma unroll
;                     for (int bj = 0; bj < 2; ++bj) { const f32x4 x1 = acc[ai][bj][m][0], x2 = acc[ai][bj][m][1]; const f32x4 o1 = x1 * cc - x2 * ss, o2 = x2 * cc + x1 * ss;
;                         u32x2 w1, w2; w1.x = cvt_pk_bf16(o1[0], o1[1]); w1.y = cvt_pk_bf16(o1[2], o1[3]); w2.x = cvt_pk_bf16(o2[0], o2[1]); w2.y = cvt_pk_bf16(o2[2], o2[3]);
;                         PG8_ST8(rsp_, P, rowp + bj * HALF, w1); PG8_ST8(rsp_, P, rowp + bj * HALF + 32, w2); } }
	global_store_dwordx4 v[206:207], v[228:231], off
	v_pk_mul_f32 v[136:137], v[174:175], v[146:147] op_sel_hi:[0,1]
	v_pk_mul_f32 v[132:133], v[174:175], v[140:141] op_sel_hi:[0,1]
	v_pk_mul_f32 v[134:135], v[174:175], v[142:143] op_sel_hi:[0,1]
	v_pk_mul_f32 v[142:143], v[36:37], v[138:139]
	v_pk_mul_f32 v[144:145], v[38:39], v[136:137]
	v_mad_i64_i32 v[140:141], s[34:35], v170, s36, v[176:177]
	v_pk_fma_f32 v[144:145], v[46:47], v[134:135], v[144:145] neg_lo:[0,0,1] neg_hi:[0,0,1]
	v_pk_fma_f32 v[142:143], v[44:45], v[132:133], v[142:143] neg_lo:[0,0,1] neg_hi:[0,0,1]
	v_pk_mul_f32 v[146:147], v[44:45], v[138:139]
	v_pk_mul_f32 v[192:193], v[46:47], v[136:137]
	v_lshl_add_u64 v[140:141], v[140:141], 0, v[178:179]
	v_pk_fma_f32 v[192:193], v[38:39], v[134:135], v[192:193]
	v_pk_fma_f32 v[146:147], v[36:37], v[132:133], v[146:147]
	v_cvt_pk_bf16_f32 v236, v142, v143
	v_cvt_pk_bf16_f32 v237, v144, v145
	s_nop 0
	v_cvt_pk_bf16_f32 v238, v146, v147
	v_cvt_pk_bf16_f32 v239, v192, v193
	s_nop 1
	v_permlane16_swap_b32_e32 v236, v238
	v_permlane16_swap_b32_e32 v237, v239
	ds_bpermute_b32 v236, v244, v236
	ds_bpermute_b32 v237, v244, v237
	ds_bpermute_b32 v238, v244, v238
	ds_bpermute_b32 v239, v244, v239
	s_waitcnt lgkmcnt(4)
	global_store_dwordx4 v[206:207], v[232:235], off offset:256
	v_pk_mul_f32 v[142:143], v[40:41], v[138:139]
	v_pk_mul_f32 v[144:145], v[42:43], v[136:137]
	v_pk_mul_f32 v[138:139], v[48:49], v[138:139]
	v_pk_mul_f32 v[136:137], v[50:51], v[136:137]
	v_pk_fma_f32 v[144:145], v[50:51], v[134:135], v[144:145] neg_lo:[0,0,1] neg_hi:[0,0,1]
	v_pk_fma_f32 v[142:143], v[48:49], v[132:133], v[142:143] neg_lo:[0,0,1] neg_hi:[0,0,1]
	v_pk_fma_f32 v[134:135], v[42:43], v[134:135], v[136:137]
	v_pk_fma_f32 v[132:133], v[40:41], v[132:133], v[138:139]
	v_cvt_pk_bf16_f32 v240, v142, v143
	v_cvt_pk_bf16_f32 v241, v144, v145
	v_pk_mul_f32 v[138:139], v[174:175], v[184:185] op_sel_hi:[0,1]
	v_cvt_pk_bf16_f32 v242, v132, v133
	v_cvt_pk_bf16_f32 v243, v134, v135
	s_nop 1
	v_permlane16_swap_b32_e32 v240, v242
	v_permlane16_swap_b32_e32 v241, v243
	ds_bpermute_b32 v240, v244, v240
	ds_bpermute_b32 v241, v244, v241
	ds_bpermute_b32 v242, v244, v242
	ds_bpermute_b32 v243, v244, v243
	s_waitcnt lgkmcnt(4)
	global_store_dwordx4 v[140:141], v[236:239], off
	v_pk_mul_f32 v[136:137], v[174:175], v[186:187] op_sel_hi:[0,1]
	v_pk_mul_f32 v[132:133], v[174:175], v[180:181] op_sel_hi:[0,1]
	v_pk_mul_f32 v[134:135], v[174:175], v[182:183] op_sel_hi:[0,1]
	v_pk_mul_f32 v[142:143], v[20:21], v[138:139]
	v_pk_mul_f32 v[144:145], v[22:23], v[136:137]
	v_mad_i64_i32 v[206:207], s[34:35], v168, s36, v[176:177]
	v_pk_fma_f32 v[144:145], v[30:31], v[134:135], v[144:145] neg_lo:[0,0,1] neg_hi:[0,0,1]
	v_pk_fma_f32 v[142:143], v[28:29], v[132:133], v[142:143] neg_lo:[0,0,1] neg_hi:[0,0,1]
	v_pk_mul_f32 v[146:147], v[28:29], v[138:139]
	v_pk_mul_f32 v[180:181], v[30:31], v[136:137]
	v_lshl_add_u64 v[206:207], v[206:207], 0, v[178:179]
	v_pk_fma_f32 v[180:181], v[22:23], v[134:135], v[180:181]
	v_pk_fma_f32 v[146:147], v[20:21], v[132:133], v[146:147]
	v_cvt_pk_bf16_f32 v228, v142, v143
	v_cvt_pk_bf16_f32 v229, v144, v145
	s_nop 0
	v_cvt_pk_bf16_f32 v230, v146, v147
	v_cvt_pk_bf16_f32 v231, v180, v181
	s_nop 1
	v_permlane16_swap_b32_e32 v228, v230
	v_permlane16_swap_b32_e32 v229, v231
	ds_bpermute_b32 v228, v244, v228
	ds_bpermute_b32 v229, v244, v229
	ds_bpermute_b32 v230, v244, v230
	ds_bpermute_b32 v231, v244, v231
	s_waitcnt lgkmcnt(4)
	global_store_dwordx4 v[140:141], v[240:243], off offset:256
	v_pk_mul_f32 v[142:143], v[24:25], v[138:139]
	v_pk_mul_f32 v[144:145], v[26:27], v[136:137]
	v_pk_mul_f32 v[138:139], v[32:33], v[138:139]
	v_pk_mul_f32 v[136:137], v[34:35], v[136:137]
	v_pk_fma_f32 v[144:145], v[34:35], v[134:135], v[144:145] neg_lo:[0,0,1] neg_hi:[0,0,1]
	v_pk_fma_f32 v[142:143], v[32:33], v[132:133], v[142:143] neg_lo:[0,0,1] neg_hi:[0,0,1]
	v_pk_fma_f32 v[134:135], v[26:27], v[134:135], v[136:137]
	v_pk_fma_f32 v[132:133], v[24:25], v[132:133], v[138:139]
	v_cvt_pk_bf16_f32 v232, v142, v143
	v_cvt_pk_bf16_f32 v233, v144, v145
	v_pk_mul_f32 v[138:139], v[174:175], v[218:219] op_sel_hi:[0,1]
	v_cvt_pk_bf16_f32 v234, v132, v133
	v_cvt_pk_bf16_f32 v235, v134, v135
	s_nop 1
	v_permlane16_swap_b32_e32 v232, v234
	v_permlane16_swap_b32_e32 v233, v235
	ds_bpermute_b32 v232, v244, v232
	ds_bpermute_b32 v233, v244, v233
	ds_bpermute_b32 v234, v244, v234
	ds_bpermute_b32 v235, v244, v235
	s_waitcnt lgkmcnt(4)
	global_store_dwordx4 v[206:207], v[228:231], off
	v_pk_mul_f32 v[136:137], v[174:175], v[220:221] op_sel_hi:[0,1]
	v_pk_mul_f32 v[132:133], v[174:175], v[188:189] op_sel_hi:[0,1]
	v_pk_mul_f32 v[134:135], v[174:175], v[190:191] op_sel_hi:[0,1]
	v_pk_mul_f32 v[142:143], v[4:5], v[138:139]
	v_pk_mul_f32 v[144:145], v[6:7], v[136:137]
	v_mad_i64_i32 v[140:141], s[34:35], v166, s36, v[176:177]
	v_pk_fma_f32 v[144:145], v[14:15], v[134:135], v[144:145] neg_lo:[0,0,1] neg_hi:[0,0,1]
	v_pk_fma_f32 v[142:143], v[12:13], v[132:133], v[142:143] neg_lo:[0,0,1] neg_hi:[0,0,1]
	v_pk_mul_f32 v[146:147], v[12:13], v[138:139]
	v_pk_mul_f32 v[176:177], v[14:15], v[136:137]
	v_lshl_add_u64 v[140:141], v[140:141], 0, v[178:179]
	v_pk_fma_f32 v[176:177], v[6:7], v[134:135], v[176:177]
	v_pk_fma_f32 v[146:147], v[4:5], v[132:133], v[146:147]
	v_cvt_pk_bf16_f32 v236, v142, v143
	v_cvt_pk_bf16_f32 v237, v144, v145
	s_mov_b64 s[34:35], 0
	v_cvt_pk_bf16_f32 v238, v146, v147
	v_cvt_pk_bf16_f32 v239, v176, v177
	s_nop 1
	v_permlane16_swap_b32_e32 v236, v238
	v_permlane16_swap_b32_e32 v237, v239
	ds_bpermute_b32 v236, v244, v236
	ds_bpermute_b32 v237, v244, v237
	ds_bpermute_b32 v238, v244, v238
	ds_bpermute_b32 v239, v244, v239
	s_waitcnt lgkmcnt(4)
	global_store_dwordx4 v[206:207], v[232:235], off offset:256
	v_pk_mul_f32 v[142:143], v[8:9], v[138:139]
	v_pk_mul_f32 v[144:145], v[10:11], v[136:137]
	v_pk_mul_f32 v[138:139], v[16:17], v[138:139]
	v_pk_mul_f32 v[136:137], v[18:19], v[136:137]
	v_pk_fma_f32 v[144:145], v[18:19], v[134:135], v[144:145] neg_lo:[0,0,1] neg_hi:[0,0,1]
	v_pk_fma_f32 v[142:143], v[16:17], v[132:133], v[142:143] neg_lo:[0,0,1] neg_hi:[0,0,1]
	v_pk_fma_f32 v[134:135], v[10:11], v[134:135], v[136:137]
	v_pk_fma_f32 v[132:133], v[8:9], v[132:133], v[138:139]
	v_cvt_pk_bf16_f32 v136, v142, v143
	v_cvt_pk_bf16_f32 v137, v144, v145
	s_nop 0
	v_cvt_pk_bf16_f32 v242, v132, v133
	v_cvt_pk_bf16_f32 v243, v134, v135
	v_mov_b32_e32 v240, v136
	v_mov_b32_e32 v241, v137
	s_nop 1
	v_permlane16_swap_b32_e32 v240, v242
	v_permlane16_swap_b32_e32 v241, v243
	ds_bpermute_b32 v240, v244, v240
	ds_bpermute_b32 v241, v244, v241
	ds_bpermute_b32 v242, v244, v242
	ds_bpermute_b32 v243, v244, v243
	s_waitcnt lgkmcnt(4)
	global_store_dwordx4 v[140:141], v[236:239], off
	s_waitcnt lgkmcnt(0)
	global_store_dwordx4 v[140:141], v[240:243], off offset:256
